# speedup vs baseline: 1.0273x; 1.0238x over previous
_Z15gemm_out_kernelPKDF16_S0_Pf:
	s_load_dwordx4 s[16:19], s[0:1], 0x0
	s_load_dwordx2 s[4:5], s[0:1], 0x10
	s_and_b32 s0, s2, 7
	s_lshr_b32 s1, s2, 3
	s_lshr_b32 s8, s0, 1
	s_lshl_b32 s8, s8, 3
	s_and_b32 s9, s1, 7
	s_or_b32 s9, s8, s9
	s_and_b32 s0, s0, 1
	s_lshl_b32 s0, s0, 2
	s_lshr_b32 s8, s1, 3
	s_or_b32 s8, s0, s8
	v_readfirstlane_b32 s10, v0
	s_lshr_b32 s13, s10, 6
	s_mov_b32 s1, 0
	s_lshl_b32 s0, s8, 1
	s_lshr_b32 s14, s10, 8
	s_lshl_b32 s2, s9, 19
	s_lshl_b64 s[6:7], s[0:1], 19
	s_lshl_b32 s0, s13, 10
	s_waitcnt lgkmcnt(0)
	s_add_u32 s2, s16, s2
	s_addc_u32 s3, s17, 0
	s_add_i32 s0, s0, 0
	v_lshlrev_b32_e32 v64, 4, v0
	s_mov_b32 m0, s0
	v_or_b32_e32 v66, 0x2000, v64
	global_load_lds_dwordx4 v64, s[2:3]
	s_add_i32 m0, s0, 0x2000
	v_mov_b32_e32 v67, 0
	s_add_u32 s6, s18, s6
	v_mov_b32_e32 v65, v67
	global_load_lds_dwordx4 v66, s[2:3]
	s_addc_u32 s7, s19, s7
	s_add_i32 m0, s0, 0x4000
	v_lshl_add_u64 v[68:69], s[6:7], 0, v[64:65]
	global_load_lds_dwordx4 v64, s[6:7]
	s_mov_b64 s[6:7], 0x2000
	v_lshl_add_u64 v[2:3], v[68:69], 0, s[6:7]
	s_add_i32 m0, s0, 0x6000
	s_mov_b64 s[16:17], 0x80000
	global_load_lds_dwordx4 v[2:3], off
	s_add_i32 m0, s0, 0x8000
	v_lshl_add_u64 v[70:71], v[68:69], 0, s[16:17]
	global_load_lds_dwordx4 v[70:71], off
	s_mov_b64 s[16:17], 0x82000
	s_add_i32 m0, s0, 0xa000
	v_lshl_add_u64 v[72:73], v[68:69], 0, s[16:17]
	s_add_u32 s18, s2, 0x4000
	global_load_lds_dwordx4 v[72:73], off
	s_addc_u32 s19, s3, 0
	s_add_i32 m0, s0, 0xc000
	s_mov_b64 s[16:17], 0x4000
	global_load_lds_dwordx4 v64, s[18:19]
	s_add_i32 m0, s0, 0xe000
	v_lshl_add_u64 v[2:3], v[68:69], 0, s[16:17]
	global_load_lds_dwordx4 v66, s[18:19]
	s_add_i32 m0, s0, 0x10000
	s_mov_b64 s[16:17], 0x6000
	global_load_lds_dwordx4 v[2:3], off
	v_lshl_add_u64 v[2:3], v[68:69], 0, s[16:17]
	s_add_i32 m0, s0, 0x12000
	s_mov_b64 s[16:17], 0x84000
	global_load_lds_dwordx4 v[2:3], off
	s_add_i32 m0, s0, 0x14000
	v_lshl_add_u64 v[2:3], v[68:69], 0, s[16:17]
	s_mov_b64 s[16:17], 0x86000
	global_load_lds_dwordx4 v[2:3], off
	v_lshl_add_u64 v[2:3], v[68:69], 0, s[16:17]
	s_add_i32 m0, s0, 0x16000
	s_mov_b32 s12, 2
	global_load_lds_dwordx4 v[2:3], off
	s_waitcnt vmcnt(6)
	s_cmp_lg_u32 s14, 1
	s_barrier
	s_cbranch_scc1 .LBB2_2
	s_barrier
